# P3 epilogue residual loads: each load instruction reads 64 contiguous bytes per row (lane fq at fq*16 + 64k) and a 4x4 quad transpose over the fq lanes with v_permlane32_swap / v_permlane16_swap resto
# baseline (speedup 1.0000x reference)
; __device__ __forceinline__ unsigned cvt_pk_bf16(float lo, float hi) { unsigned r; asm volatile("v_cvt_pk_bf16_f32 %0, %1, %2" : "=v"(r) : "v"(lo), "v"(hi)); return r; }
;     __device__ __forceinline__ void operator()(const f32x4 (&acc)[2][2][4][2], const pg8::Unit& u, int wr, int wc, int fr, int fq) const {
;         const int row0 = u.pm * 256 + wr * 64 + fr, col0 = u.pn * 256 + wc * 64 + 16 * fq;
; #pragma unroll
;         for (int ai = 0; ai < 2; ++ai) {
;             f32x4 b0[4][2], b1[4][2];
; #pragma unroll
;             for (int m = 0; m < 4; ++m)
; #pragma unroll
;                 for (int bj = 0; bj < 2; ++bj) { const size_t off = (size_t)(row0 + ai * 128 + m * 16) * D + col0 + bj * 8;
;                     if (BASE_F32) { b0[m][bj] = *(const f32x4*)((const float*)base + off); b1[m][bj] = *(const f32x4*)((const float*)base + off + 4); }
;                     else { const u32x4 w = *(const u32x4*)((const bf16*)base + off); b0[m][bj] = (f32x4){bflo(w.x), bfhi(w.x), bflo(w.y), bfhi(w.y)}; b1[m][bj] = (f32x4){bflo(w.z), bfhi(w.z), bflo(w.w), bfhi(w.w)}; } }
;             asm volatile("" ::: "memory");
; #pragma unroll
;             for (int m = 0; m < 4; ++m) { const int row = row0 + ai * 128 + m * 16; float ss = 0.f;
;                 u32x4 q;
; #pragma unroll
;                 for (int bj = 0; bj < 2; ++bj) { const size_t off = (size_t)row * D + col0 + bj * 8;
;                     const float asc = BASE_F32 ? 1.0f : (1.0f / 256.0f);
;                     const f32x4 v0 = acc[ai][bj][m][0] * asc + b0[m][bj], v1 = acc[ai][bj][m][1] * asc + b1[m][bj];
;                     ss += (v0[0] * v0[0] + v0[1] * v0[1]) + (v0[2] * v0[2] + v0[3] * v0[3]) + (v1[0] * v1[0] + v1[1] * v1[1]) + (v1[2] * v1[2] + v1[3] * v1[3]);
;                     u32x4 w; w.x = cvt_pk_bf16(v0[0], v0[1]); w.y = cvt_pk_bf16(v0[2], v0[3]); w.z = cvt_pk_bf16(v1[0], v1[1]); w.w = cvt_pk_bf16(v1[2], v1[3]);
;                     *(u32x4*)(out + off) = w;
;                     if (BASE_F32) { const unsigned qa = pk4_fp8(v0[0], v0[1], v0[2], v0[3]), qb = pk4_fp8(v1[0], v1[1], v1[2], v1[3]); if (bj == 0) { q.x = qa; q.y = qb; } else { q.z = qa; q.w = qb; } } }
;                 if (BASE_F32) *(u32x4*)(q8 + (size_t)row * D + col0) = q;
;                 ss += __shfl_xor(ss, 16); ss += __shfl_xor(ss, 32);
;                 if (fq == 0) ssq[(size_t)row * 16 + u.pn * 4 + wc] = ss; }
.LBB0_554:
	s_lshl_b32 s2, s19, 8
	v_mov_b32_e32 v130, v0
	s_add_i32 s2, s2, s42
	v_and_or_b32 v182, v130, 15, s2
	s_lshl_b32 s2, s15, 8
	v_bfe_u32 v179, v130, 4, 2
	s_or_b32 s2, s2, s43
	v_lshl_or_b32 v180, v179, 4, s2
	v_ashrrev_i32_e32 v181, 31, v180
	v_ashrrev_i32_e32 v183, 31, v182
	v_lshl_add_u64 v[184:185], v[180:181], 2, s[16:17]
	v_mul_i32_i24_e32 v252, 0xffffffd0, v179
	v_ashrrev_i32_e32 v253, 31, v252
	v_lshl_add_u64 v[184:185], v[184:185], 0, v[252:253]
	v_lshlrev_b64 v[130:131], 12, v[182:183]
	v_lshl_add_u64 v[130:131], v[184:185], 0, v[130:131]
	global_load_dwordx4 v[198:201], v[130:131], off
	global_load_dwordx4 v[202:205], v[130:131], off offset:64
	global_load_dwordx4 v[206:209], v[130:131], off offset:128
	global_load_dwordx4 v[210:213], v[130:131], off offset:192
	v_or_b32_e32 v190, 16, v182
	v_or_b32_e32 v188, 32, v182
	v_or_b32_e32 v186, 48, v182
	v_ashrrev_i32_e32 v191, 31, v190
	v_ashrrev_i32_e32 v189, 31, v188
	v_ashrrev_i32_e32 v187, 31, v186
	v_lshlrev_b64 v[130:131], 12, v[190:191]
	v_lshlrev_b64 v[132:133], 12, v[188:189]
	v_lshlrev_b64 v[134:135], 12, v[186:187]
	v_lshl_add_u64 v[130:131], v[184:185], 0, v[130:131]
	v_lshl_add_u64 v[132:133], v[184:185], 0, v[132:133]
	v_lshl_add_u64 v[142:143], v[184:185], 0, v[134:135]
	global_load_dwordx4 v[162:165], v[130:131], off offset:192
	global_load_dwordx4 v[166:169], v[130:131], off offset:128
	global_load_dwordx4 v[170:173], v[130:131], off offset:64
	global_load_dwordx4 v[174:177], v[130:131], off
	global_load_dwordx4 v[146:149], v[132:133], off offset:192
	global_load_dwordx4 v[150:153], v[132:133], off offset:128
	global_load_dwordx4 v[154:157], v[132:133], off offset:64
	global_load_dwordx4 v[158:161], v[132:133], off
	s_nop 0
	global_load_dwordx4 v[130:133], v[142:143], off offset:192
	global_load_dwordx4 v[134:137], v[142:143], off offset:128
	global_load_dwordx4 v[138:141], v[142:143], off offset:64
	s_nop 0
	global_load_dwordx4 v[142:145], v[142:143], off
	v_lshlrev_b64 v[216:217], 11, v[182:183]
	v_cmp_eq_u32_e32 vcc, 0, v179
	v_lshl_add_u64 v[216:217], s[24:25], 0, v[216:217]
	v_lshl_add_u64 v[218:219], v[180:181], 1, v[216:217]
	s_lshl_b32 s34, s15, 2
	s_ashr_i32 s35, s34, 31
	s_waitcnt vmcnt(12)
	s_nop 4
	v_permlane32_swap_b32_e32 v198, v206
	v_permlane32_swap_b32_e32 v199, v207
	v_permlane32_swap_b32_e32 v200, v208
	v_permlane32_swap_b32_e32 v201, v209
	v_permlane32_swap_b32_e32 v202, v210
	v_permlane32_swap_b32_e32 v203, v211
	v_permlane32_swap_b32_e32 v204, v212
	v_permlane32_swap_b32_e32 v205, v213
	s_nop 1
	v_permlane16_swap_b32_e32 v198, v202
	v_permlane16_swap_b32_e32 v199, v203
	v_permlane16_swap_b32_e32 v200, v204
	v_permlane16_swap_b32_e32 v201, v205
	v_permlane16_swap_b32_e32 v206, v210
	v_permlane16_swap_b32_e32 v207, v211
	v_permlane16_swap_b32_e32 v208, v212
	v_permlane16_swap_b32_e32 v209, v213
	s_nop 1
	s_waitcnt vmcnt(15)
	v_pk_add_f32 v[200:201], v[116:117], v[200:201]
	v_pk_add_f32 v[198:199], v[114:115], v[198:199]
	s_waitcnt vmcnt(14)
	v_pk_add_f32 v[118:119], v[118:119], v[202:203]
	s_waitcnt vmcnt(13)
	v_pk_add_f32 v[128:129], v[128:129], v[208:209]
	v_pk_add_f32 v[126:127], v[126:127], v[206:207]
	s_waitcnt vmcnt(12)
	v_pk_add_f32 v[122:123], v[122:123], v[210:211]
	v_mul_f32_e32 v179, v199, v199
	v_mul_f32_e32 v202, v201, v201
	v_mul_f32_e32 v203, v119, v119
	v_cvt_pk_bf16_f32 v114, v198, v199
	v_cvt_pk_bf16_f32 v115, v200, v201
	v_cvt_pk_bf16_f32 v116, v118, v119
	v_cvt_pk_fp8_f32 v214, v198, v199
	v_cvt_pk_fp8_f32 v215, v118, v119
	v_mul_f32_e32 v119, v127, v127
	v_mul_f32_e32 v199, v129, v129
	v_pk_add_f32 v[120:121], v[120:121], v[204:205]
	v_pk_add_f32 v[124:125], v[124:125], v[212:213]
	v_cvt_pk_bf16_f32 v117, v120, v121
	v_mul_f32_e32 v205, v123, v123
	v_fmac_f32_e32 v179, v198, v198
	v_fmac_f32_e32 v202, v200, v200
	v_fmac_f32_e32 v119, v126, v126
	v_fmac_f32_e32 v199, v128, v128
	v_mul_f32_e32 v204, v121, v121
	v_mul_f32_e32 v206, v125, v125
	v_fmac_f32_e32 v203, v118, v118
	global_store_dwordx4 v[218:219], v[114:117], off
	v_fmac_f32_e32 v205, v122, v122
	v_add_f32_e32 v118, v119, v199
	v_add_f32_e32 v117, v179, v202
	v_fmac_f32_e32 v204, v120, v120
	v_fmac_f32_e32 v206, v124, v124
	v_add_f32_e32 v117, v117, v203
	v_add_f32_e32 v118, v118, v205
	v_add_f32_e32 v117, v204, v117
	v_add_f32_e32 v118, v206, v118
	v_and_b32_e32 v119, 64, v197
	v_add_f32_e32 v118, v117, v118
	v_xor_b32_e32 v117, 16, v197
	v_add_u32_e32 v119, 64, v119
	v_cmp_lt_i32_e64 s[2:3], v117, v119
	v_cvt_pk_bf16_f32 v114, v126, v127
	v_cvt_pk_bf16_f32 v115, v128, v129
	v_cvt_pk_bf16_f32 v116, v122, v123
	v_cvt_pk_fp8_f32 v217, v122, v123
	v_cvt_pk_fp8_f32 v215, v120, v121 op_sel:[0,0,1]
	v_cndmask_b32_e64 v117, v197, v117, s[2:3]
	v_lshlrev_b32_e32 v122, 2, v117
	ds_bpermute_b32 v120, v122, v118
	v_cvt_pk_bf16_f32 v117, v124, v125
	global_store_dwordx4 v[218:219], v[114:117], off offset:16
	v_cvt_pk_fp8_f32 v216, v126, v127
	v_cvt_pk_fp8_f32 v214, v200, v201 op_sel:[0,0,1]
	v_xor_b32_e32 v115, 32, v197
	v_cmp_lt_i32_e64 s[2:3], v115, v119
	s_waitcnt lgkmcnt(0)
	v_add_f32_e32 v114, v118, v120
	v_cvt_pk_fp8_f32 v216, v128, v129 op_sel:[0,0,1]
	v_cndmask_b32_e64 v115, v197, v115, s[2:3]
	v_lshlrev_b32_e32 v123, 2, v115
	ds_bpermute_b32 v115, v123, v114
	v_cvt_pk_fp8_f32 v217, v124, v125 op_sel:[0,0,1]
	v_lshlrev_b64 v[116:117], 10, v[182:183]
	v_lshl_add_u64 v[116:117], s[28:29], 0, v[116:117]
	v_lshl_add_u64 v[116:117], v[116:117], 0, v[180:181]
	global_store_dwordx4 v[116:117], v[214:217], off
	s_and_saveexec_b64 s[2:3], vcc
	s_cbranch_execz .LBB0_556
	v_lshlrev_b64 v[116:117], 6, v[182:183]
	v_lshl_add_u64 v[116:117], s[26:27], 0, v[116:117]
	v_lshl_add_u64 v[116:117], s[34:35], 2, v[116:117]
	s_lshl_b32 s20, s7, 2
	v_lshl_add_u64 v[116:117], v[116:117], 0, s[20:21]
	s_waitcnt lgkmcnt(0)
	v_add_f32_e32 v114, v114, v115
	global_store_dword v[116:117], v114, off
; __device__ __forceinline__ unsigned cvt_pk_bf16(float lo, float hi) { unsigned r; asm volatile("v_cvt_pk_bf16_f32 %0, %1, %2" : "=v"(r) : "v"(lo), "v"(hi)); return r; }
; __device__ __forceinline__ unsigned pk4_fp8(float a, float b, float c, float d) { int w = __builtin_amdgcn_cvt_pk_fp8_f32(a, b, 0, false); w = __builtin_amdgcn_cvt_pk_fp8_f32(c, d, w, true); return (unsigned)w; }
;     __device__ __forceinline__ void operator()(const f32x4 (&acc)[2][2][4][2], const pg8::Unit& u, int wr, int wc, int fr, int fq) const {
;     ...
; #pragma unroll
;             for (int m = 0; m < 4; ++m) { const int row = row0 + ai * 128 + m * 16; float ss = 0.f;
;                 u32x4 q;
; #pragma unroll
;                 for (int bj = 0; bj < 2; ++bj) { const size_t off = (size_t)row * D + col0 + bj * 8;
;                     const float asc = BASE_F32 ? 1.0f : (1.0f / 256.0f);
;                     const f32x4 v0 = acc[ai][bj][m][0] * asc + b0[m][bj], v1 = acc[ai][bj][m][1] * asc + b1[m][bj];
;                     ss += (v0[0] * v0[0] + v0[1] * v0[1]) + (v0[2] * v0[2] + v0[3] * v0[3]) + (v1[0] * v1[0] + v1[1] * v1[1]) + (v1[2] * v1[2] + v1[3] * v1[3]);
;                     u32x4 w; w.x = cvt_pk_bf16(v0[0], v0[1]); w.y = cvt_pk_bf16(v0[2], v0[3]); w.z = cvt_pk_bf16(v1[0], v1[1]); w.w = cvt_pk_bf16(v1[2], v1[3]);
;                     *(u32x4*)(out + off) = w;
;                     if (BASE_F32) { const unsigned qa = pk4_fp8(v0[0], v0[1], v0[2], v0[3]), qb = pk4_fp8(v1[0], v1[1], v1[2], v1[3]); if (bj == 0) { q.x = qa; q.y = qb; } else { q.z = qa; q.w = qb; } } }
;                 if (BASE_F32) *(u32x4*)(q8 + (size_t)row * D + col0) = q;
;                 ss += __shfl_xor(ss, 16); ss += __shfl_xor(ss, 32);
;                 if (fq == 0) ssq[(size_t)row * 16 + u.pn * 4 + wc] = ss; }
.LBB0_556:
	s_or_b64 exec, exec, s[2:3]
	s_waitcnt vmcnt(11)
	s_nop 4
	v_permlane32_swap_b32_e32 v174, v166
	v_permlane32_swap_b32_e32 v175, v167
	v_permlane32_swap_b32_e32 v176, v168
	v_permlane32_swap_b32_e32 v177, v169
	v_permlane32_swap_b32_e32 v170, v162
	v_permlane32_swap_b32_e32 v171, v163
	v_permlane32_swap_b32_e32 v172, v164
	v_permlane32_swap_b32_e32 v173, v165
	s_nop 1
	v_permlane16_swap_b32_e32 v174, v170
	v_permlane16_swap_b32_e32 v175, v171
	v_permlane16_swap_b32_e32 v176, v172
	v_permlane16_swap_b32_e32 v177, v173
	v_permlane16_swap_b32_e32 v166, v162
	v_permlane16_swap_b32_e32 v167, v163
	v_permlane16_swap_b32_e32 v168, v164
	v_permlane16_swap_b32_e32 v169, v165
	s_nop 1
	v_pk_add_f32 v[112:113], v[112:113], v[176:177]
	v_pk_add_f32 v[116:117], v[110:111], v[174:175]
	v_pk_add_f32 v[120:121], v[106:107], v[170:171]
	v_mul_f32_e32 v106, v117, v117
	v_mul_f32_e32 v107, v113, v113
	v_fmac_f32_e32 v106, v116, v116
	v_fmac_f32_e32 v107, v112, v112
	v_add_f32_e32 v106, v106, v107
	v_mul_f32_e32 v107, v121, v121
	v_pk_add_f32 v[118:119], v[108:109], v[172:173]
	v_fmac_f32_e32 v107, v120, v120
	s_waitcnt lgkmcnt(0)
	v_lshlrev_b64 v[114:115], 11, v[190:191]
	v_add_f32_e32 v106, v106, v107
	v_mul_f32_e32 v107, v119, v119
	v_fmac_f32_e32 v107, v118, v118
	v_lshl_add_u64 v[114:115], s[24:25], 0, v[114:115]
	v_add_f32_e32 v124, v107, v106
	v_cvt_pk_bf16_f32 v106, v116, v117
	v_cvt_pk_bf16_f32 v107, v112, v113
	v_cvt_pk_bf16_f32 v108, v120, v121
	v_cvt_pk_bf16_f32 v109, v118, v119
	v_lshl_add_u64 v[114:115], v[180:181], 1, v[114:115]
	v_pk_add_f32 v[104:105], v[104:105], v[168:169]
	v_pk_add_f32 v[102:103], v[102:103], v[166:167]
	global_store_dwordx4 v[114:115], v[106:109], off
	v_cvt_pk_fp8_f32 v110, v116, v117
	v_pk_add_f32 v[108:109], v[98:99], v[162:163]
	v_mul_f32_e32 v98, v103, v103
	v_mul_f32_e32 v99, v105, v105
	v_fmac_f32_e32 v98, v102, v102
	v_fmac_f32_e32 v99, v104, v104
	v_add_f32_e32 v98, v98, v99
	v_mul_f32_e32 v99, v109, v109
	v_pk_add_f32 v[106:107], v[100:101], v[164:165]
	v_fmac_f32_e32 v99, v108, v108
	v_add_f32_e32 v98, v98, v99
	v_mul_f32_e32 v99, v107, v107
	v_fmac_f32_e32 v99, v106, v106
	v_add_f32_e32 v98, v99, v98
	v_cvt_pk_fp8_f32 v110, v112, v113 op_sel:[0,0,1]
	v_add_f32_e32 v116, v124, v98
	v_cvt_pk_bf16_f32 v98, v102, v103
	v_cvt_pk_fp8_f32 v112, v102, v103
	ds_bpermute_b32 v102, v122, v116
	v_cvt_pk_fp8_f32 v111, v120, v121
	v_cvt_pk_fp8_f32 v113, v108, v109
	v_cvt_pk_bf16_f32 v99, v104, v105
	v_cvt_pk_bf16_f32 v100, v108, v109
	v_cvt_pk_bf16_f32 v101, v106, v107
	global_store_dwordx4 v[114:115], v[98:101], off offset:16
	v_cvt_pk_fp8_f32 v111, v118, v119 op_sel:[0,0,1]
	v_cvt_pk_fp8_f32 v112, v104, v105 op_sel:[0,0,1]
	s_waitcnt lgkmcnt(0)
	v_add_f32_e32 v98, v116, v102
	ds_bpermute_b32 v99, v123, v98
	v_cvt_pk_fp8_f32 v113, v106, v107 op_sel:[0,0,1]
	v_lshlrev_b64 v[100:101], 10, v[190:191]
	v_lshl_add_u64 v[100:101], s[28:29], 0, v[100:101]
	v_lshl_add_u64 v[100:101], v[100:101], 0, v[180:181]
	global_store_dwordx4 v[100:101], v[110:113], off
	s_and_saveexec_b64 s[2:3], vcc
	s_cbranch_execz .LBB0_558
	v_lshlrev_b64 v[100:101], 6, v[190:191]
	v_lshl_add_u64 v[100:101], s[26:27], 0, v[100:101]
	v_lshl_add_u64 v[100:101], s[34:35], 2, v[100:101]
	s_lshl_b32 s20, s7, 2
	v_lshl_add_u64 v[100:101], v[100:101], 0, s[20:21]
	s_waitcnt lgkmcnt(0)
	v_add_f32_e32 v98, v98, v99
	global_store_dword v[100:101], v98, off
.LBB0_558:
	s_or_b64 exec, exec, s[2:3]
	s_waitcnt vmcnt(10)
	s_nop 4
	v_permlane32_swap_b32_e32 v158, v150
	v_permlane32_swap_b32_e32 v159, v151
	v_permlane32_swap_b32_e32 v160, v152
	v_permlane32_swap_b32_e32 v161, v153
	v_permlane32_swap_b32_e32 v154, v146
	v_permlane32_swap_b32_e32 v155, v147
	v_permlane32_swap_b32_e32 v156, v148
	v_permlane32_swap_b32_e32 v157, v149
	s_nop 1
	v_permlane16_swap_b32_e32 v158, v154
	v_permlane16_swap_b32_e32 v159, v155
	v_permlane16_swap_b32_e32 v160, v156
	v_permlane16_swap_b32_e32 v161, v157
	v_permlane16_swap_b32_e32 v150, v146
	v_permlane16_swap_b32_e32 v151, v147
	v_permlane16_swap_b32_e32 v152, v148
	v_permlane16_swap_b32_e32 v153, v149
	s_nop 1
	v_pk_add_f32 v[96:97], v[96:97], v[160:161]
	v_pk_add_f32 v[100:101], v[94:95], v[158:159]
	v_pk_add_f32 v[104:105], v[90:91], v[154:155]
	v_mul_f32_e32 v90, v101, v101
	v_mul_f32_e32 v91, v97, v97
	v_fmac_f32_e32 v90, v100, v100
	v_fmac_f32_e32 v91, v96, v96
	v_add_f32_e32 v90, v90, v91
	v_mul_f32_e32 v91, v105, v105
	v_pk_add_f32 v[102:103], v[92:93], v[156:157]
	v_fmac_f32_e32 v91, v104, v104
	s_waitcnt lgkmcnt(0)
	v_lshlrev_b64 v[98:99], 11, v[188:189]
	v_add_f32_e32 v90, v90, v91
	v_mul_f32_e32 v91, v103, v103
	v_fmac_f32_e32 v91, v102, v102
	v_lshl_add_u64 v[98:99], s[24:25], 0, v[98:99]
	v_add_f32_e32 v106, v91, v90
	v_cvt_pk_bf16_f32 v90, v100, v101
	v_cvt_pk_bf16_f32 v91, v96, v97
	v_cvt_pk_bf16_f32 v92, v104, v105
	v_cvt_pk_bf16_f32 v93, v102, v103
	v_lshl_add_u64 v[98:99], v[180:181], 1, v[98:99]
	v_pk_add_f32 v[88:89], v[88:89], v[152:153]
	v_pk_add_f32 v[86:87], v[86:87], v[150:151]
	global_store_dwordx4 v[98:99], v[90:93], off
	v_cvt_pk_fp8_f32 v94, v100, v101
	v_pk_add_f32 v[92:93], v[82:83], v[146:147]
	v_mul_f32_e32 v82, v87, v87
	v_mul_f32_e32 v83, v89, v89
	v_fmac_f32_e32 v82, v86, v86
	v_fmac_f32_e32 v83, v88, v88
	v_add_f32_e32 v82, v82, v83
	v_mul_f32_e32 v83, v93, v93
	v_pk_add_f32 v[90:91], v[84:85], v[148:149]
	v_fmac_f32_e32 v83, v92, v92
	v_add_f32_e32 v82, v82, v83
	v_mul_f32_e32 v83, v91, v91
	v_fmac_f32_e32 v83, v90, v90
	v_add_f32_e32 v82, v83, v82
	v_cvt_pk_fp8_f32 v94, v96, v97 op_sel:[0,0,1]
	v_add_f32_e32 v100, v106, v82
	v_cvt_pk_bf16_f32 v82, v86, v87
	v_cvt_pk_fp8_f32 v96, v86, v87
	ds_bpermute_b32 v86, v122, v100
	v_cvt_pk_fp8_f32 v95, v104, v105
	v_cvt_pk_fp8_f32 v97, v92, v93
	v_cvt_pk_bf16_f32 v83, v88, v89
	v_cvt_pk_bf16_f32 v84, v92, v93
	v_cvt_pk_bf16_f32 v85, v90, v91
	global_store_dwordx4 v[98:99], v[82:85], off offset:16
	v_cvt_pk_fp8_f32 v95, v102, v103 op_sel:[0,0,1]
	v_cvt_pk_fp8_f32 v96, v88, v89 op_sel:[0,0,1]
	s_waitcnt lgkmcnt(0)
	v_add_f32_e32 v82, v100, v86
	ds_bpermute_b32 v83, v123, v82
	v_cvt_pk_fp8_f32 v97, v90, v91 op_sel:[0,0,1]
	v_lshlrev_b64 v[84:85], 10, v[188:189]
	v_lshl_add_u64 v[84:85], s[28:29], 0, v[84:85]
	v_lshl_add_u64 v[84:85], v[84:85], 0, v[180:181]
	global_store_dwordx4 v[84:85], v[94:97], off
	s_and_saveexec_b64 s[2:3], vcc
	s_cbranch_execz .LBB0_560
	v_lshlrev_b64 v[84:85], 6, v[188:189]
	v_lshl_add_u64 v[84:85], s[26:27], 0, v[84:85]
	v_lshl_add_u64 v[84:85], s[34:35], 2, v[84:85]
	s_lshl_b32 s20, s7, 2
	v_lshl_add_u64 v[84:85], v[84:85], 0, s[20:21]
	s_waitcnt lgkmcnt(0)
	v_add_f32_e32 v82, v82, v83
	global_store_dword v[84:85], v82, off
; __device__ __forceinline__ unsigned cvt_pk_bf16(float lo, float hi) { unsigned r; asm volatile("v_cvt_pk_bf16_f32 %0, %1, %2" : "=v"(r) : "v"(lo), "v"(hi)); return r; }
;     __device__ __forceinline__ void operator()(const f32x4 (&acc)[2][2][4][2], const pg8::Unit& u, int wr, int wc, int fr, int fq) const {
;     ...
;         for (int ai = 0; ai < 2; ++ai) {
;             f32x4 b0[4][2], b1[4][2];
; #pragma unroll
;             for (int m = 0; m < 4; ++m)
; #pragma unroll
;                 for (int bj = 0; bj < 2; ++bj) { const size_t off = (size_t)(row0 + ai * 128 + m * 16) * D + col0 + bj * 8;
;                     if (BASE_F32) { b0[m][bj] = *(const f32x4*)((const float*)base + off); b1[m][bj] = *(const f32x4*)((const float*)base + off + 4); }
;                     else { const u32x4 w = *(const u32x4*)((const bf16*)base + off); b0[m][bj] = (f32x4){bflo(w.x), bfhi(w.x), bflo(w.y), bfhi(w.y)}; b1[m][bj] = (f32x4){bflo(w.z), bfhi(w.z), bflo(w.w), bfhi(w.w)}; } }
;             asm volatile("" ::: "memory");
; #pragma unroll
;             for (int m = 0; m < 4; ++m) { const int row = row0 + ai * 128 + m * 16; float ss = 0.f;
;                 u32x4 q;
; #pragma unroll
;                 for (int bj = 0; bj < 2; ++bj) { const size_t off = (size_t)row * D + col0 + bj * 8;
;                     const float asc = BASE_F32 ? 1.0f : (1.0f / 256.0f);
;                     const f32x4 v0 = acc[ai][bj][m][0] * asc + b0[m][bj], v1 = acc[ai][bj][m][1] * asc + b1[m][bj];
;                     ss += (v0[0] * v0[0] + v0[1] * v0[1]) + (v0[2] * v0[2] + v0[3] * v0[3]) + (v1[0] * v1[0] + v1[1] * v1[1]) + (v1[2] * v1[2] + v1[3] * v1[3]);
;                     u32x4 w; w.x = cvt_pk_bf16(v0[0], v0[1]); w.y = cvt_pk_bf16(v0[2], v0[3]); w.z = cvt_pk_bf16(v1[0], v1[1]); w.w = cvt_pk_bf16(v1[2], v1[3]);
;                     *(u32x4*)(out + off) = w;
;                     if (BASE_F32) { const unsigned qa = pk4_fp8(v0[0], v0[1], v0[2], v0[3]), qb = pk4_fp8(v1[0], v1[1], v1[2], v1[3]); if (bj == 0) { q.x = qa; q.y = qb; } else { q.z = qa; q.w = qb; } } }
;                 if (BASE_F32) *(u32x4*)(q8 + (size_t)row * D + col0) = q;
;                 ss += __shfl_xor(ss, 16); ss += __shfl_xor(ss, 32);
;                 if (fq == 0) ssq[(size_t)row * 16 + u.pn * 4 + wc] = ss; }
.LBB0_560:
	s_or_b64 exec, exec, s[2:3]
	s_waitcnt vmcnt(9)
	s_nop 4
	v_permlane32_swap_b32_e32 v142, v134
	v_permlane32_swap_b32_e32 v143, v135
	v_permlane32_swap_b32_e32 v144, v136
	v_permlane32_swap_b32_e32 v145, v137
	v_permlane32_swap_b32_e32 v138, v130
	v_permlane32_swap_b32_e32 v139, v131
	v_permlane32_swap_b32_e32 v140, v132
	v_permlane32_swap_b32_e32 v141, v133
	s_nop 1
	v_permlane16_swap_b32_e32 v142, v138
	v_permlane16_swap_b32_e32 v143, v139
	v_permlane16_swap_b32_e32 v144, v140
	v_permlane16_swap_b32_e32 v145, v141
	v_permlane16_swap_b32_e32 v134, v130
	v_permlane16_swap_b32_e32 v135, v131
	v_permlane16_swap_b32_e32 v136, v132
	v_permlane16_swap_b32_e32 v137, v133
	s_nop 1
	v_pk_add_f32 v[80:81], v[80:81], v[144:145]
	v_pk_add_f32 v[84:85], v[78:79], v[142:143]
	v_pk_add_f32 v[88:89], v[74:75], v[138:139]
	v_mul_f32_e32 v74, v85, v85
	v_mul_f32_e32 v75, v81, v81
	v_fmac_f32_e32 v74, v84, v84
	v_fmac_f32_e32 v75, v80, v80
	v_add_f32_e32 v74, v74, v75
	v_mul_f32_e32 v75, v89, v89
	v_pk_add_f32 v[86:87], v[76:77], v[140:141]
	v_fmac_f32_e32 v75, v88, v88
	s_waitcnt lgkmcnt(0)
	v_lshlrev_b64 v[82:83], 11, v[186:187]
	v_add_f32_e32 v74, v74, v75
	v_mul_f32_e32 v75, v87, v87
	v_fmac_f32_e32 v75, v86, v86
	v_lshl_add_u64 v[82:83], s[24:25], 0, v[82:83]
	v_add_f32_e32 v90, v75, v74
	v_cvt_pk_bf16_f32 v74, v84, v85
	v_cvt_pk_bf16_f32 v75, v80, v81
	v_cvt_pk_bf16_f32 v76, v88, v89
	v_cvt_pk_bf16_f32 v77, v86, v87
	v_lshl_add_u64 v[82:83], v[180:181], 1, v[82:83]
	v_pk_add_f32 v[72:73], v[72:73], v[136:137]
	v_pk_add_f32 v[70:71], v[70:71], v[134:135]
	global_store_dwordx4 v[82:83], v[74:77], off
	v_cvt_pk_fp8_f32 v78, v84, v85
	v_pk_add_f32 v[76:77], v[66:67], v[130:131]
	v_mul_f32_e32 v66, v71, v71
	v_mul_f32_e32 v67, v73, v73
	v_fmac_f32_e32 v66, v70, v70
	v_fmac_f32_e32 v67, v72, v72
	v_add_f32_e32 v66, v66, v67
	v_mul_f32_e32 v67, v77, v77
	v_pk_add_f32 v[74:75], v[68:69], v[132:133]
	v_fmac_f32_e32 v67, v76, v76
	v_add_f32_e32 v66, v66, v67
	v_mul_f32_e32 v67, v75, v75
	v_fmac_f32_e32 v67, v74, v74
	v_add_f32_e32 v66, v67, v66
	v_cvt_pk_fp8_f32 v78, v80, v81 op_sel:[0,0,1]
	v_add_f32_e32 v84, v90, v66
	v_cvt_pk_bf16_f32 v66, v70, v71
	v_cvt_pk_fp8_f32 v80, v70, v71
	ds_bpermute_b32 v70, v122, v84
	v_cvt_pk_fp8_f32 v79, v88, v89
	v_cvt_pk_fp8_f32 v81, v76, v77
	v_cvt_pk_bf16_f32 v67, v72, v73
	v_cvt_pk_bf16_f32 v68, v76, v77
	v_cvt_pk_bf16_f32 v69, v74, v75
	global_store_dwordx4 v[82:83], v[66:69], off offset:16
	v_cvt_pk_fp8_f32 v79, v86, v87 op_sel:[0,0,1]
	v_cvt_pk_fp8_f32 v80, v72, v73 op_sel:[0,0,1]
	s_waitcnt lgkmcnt(0)
	v_add_f32_e32 v66, v84, v70
	ds_bpermute_b32 v67, v123, v66
	v_cvt_pk_fp8_f32 v81, v74, v75 op_sel:[0,0,1]
	v_lshlrev_b64 v[68:69], 10, v[186:187]
	v_lshl_add_u64 v[68:69], s[28:29], 0, v[68:69]
	v_lshl_add_u64 v[68:69], v[68:69], 0, v[180:181]
	global_store_dwordx4 v[68:69], v[78:81], off
	s_and_saveexec_b64 s[2:3], vcc
	s_cbranch_execz .LBB0_562
	v_lshlrev_b64 v[68:69], 6, v[186:187]
	v_lshl_add_u64 v[68:69], s[26:27], 0, v[68:69]
	v_lshl_add_u64 v[68:69], s[34:35], 2, v[68:69]
	s_lshl_b32 s20, s7, 2
	v_lshl_add_u64 v[68:69], v[68:69], 0, s[20:21]
	s_waitcnt lgkmcnt(0)
	v_add_f32_e32 v66, v66, v67
	global_store_dword v[68:69], v66, off
.LBB0_562:
	s_or_b64 exec, exec, s[2:3]
	v_add_u32_e32 v120, 0x80, v182
	v_ashrrev_i32_e32 v121, 31, v120
	s_waitcnt lgkmcnt(0)
	v_lshlrev_b64 v[66:67], 12, v[120:121]
	v_lshl_add_u64 v[66:67], v[184:185], 0, v[66:67]
	global_load_dwordx4 v[124:127], v[66:67], off
	global_load_dwordx4 v[128:131], v[66:67], off offset:64
	global_load_dwordx4 v[132:135], v[66:67], off offset:128
	global_load_dwordx4 v[136:139], v[66:67], off offset:192
	v_add_u32_e32 v118, 0x90, v182
	v_add_u32_e32 v116, 0xa0, v182
	v_add_u32_e32 v114, 0xb0, v182
	v_ashrrev_i32_e32 v119, 31, v118
	v_ashrrev_i32_e32 v117, 31, v116
	v_ashrrev_i32_e32 v115, 31, v114
	v_lshlrev_b64 v[66:67], 12, v[118:119]
	v_lshlrev_b64 v[68:69], 12, v[116:117]
	v_lshlrev_b64 v[70:71], 12, v[114:115]
	v_lshl_add_u64 v[66:67], v[184:185], 0, v[66:67]
	v_lshl_add_u64 v[68:69], v[184:185], 0, v[68:69]
	v_lshl_add_u64 v[78:79], v[184:185], 0, v[70:71]
	global_load_dwordx4 v[98:101], v[66:67], off offset:192
	global_load_dwordx4 v[102:105], v[66:67], off offset:128
	global_load_dwordx4 v[106:109], v[66:67], off offset:64
	global_load_dwordx4 v[110:113], v[66:67], off
	global_load_dwordx4 v[82:85], v[68:69], off offset:192
	global_load_dwordx4 v[86:89], v[68:69], off offset:128
	global_load_dwordx4 v[90:93], v[68:69], off offset:64
	global_load_dwordx4 v[94:97], v[68:69], off
	s_nop 0
	global_load_dwordx4 v[66:69], v[78:79], off offset:192
	global_load_dwordx4 v[70:73], v[78:79], off offset:128
	global_load_dwordx4 v[74:77], v[78:79], off offset:64
	s_nop 0
	global_load_dwordx4 v[78:81], v[78:79], off
	v_lshlrev_b64 v[144:145], 11, v[120:121]
	v_lshl_add_u64 v[144:145], s[24:25], 0, v[144:145]
	v_lshl_add_u64 v[144:145], v[180:181], 1, v[144:145]
	s_waitcnt vmcnt(12)
	s_nop 4
	v_permlane32_swap_b32_e32 v124, v132
	v_permlane32_swap_b32_e32 v125, v133
	v_permlane32_swap_b32_e32 v126, v134
	v_permlane32_swap_b32_e32 v127, v135
	v_permlane32_swap_b32_e32 v128, v136
	v_permlane32_swap_b32_e32 v129, v137
	v_permlane32_swap_b32_e32 v130, v138
	v_permlane32_swap_b32_e32 v131, v139
	s_nop 1
	v_permlane16_swap_b32_e32 v124, v128
	v_permlane16_swap_b32_e32 v125, v129
	v_permlane16_swap_b32_e32 v126, v130
	v_permlane16_swap_b32_e32 v127, v131
	v_permlane16_swap_b32_e32 v132, v136
	v_permlane16_swap_b32_e32 v133, v137
	v_permlane16_swap_b32_e32 v134, v138
	v_permlane16_swap_b32_e32 v135, v139
	s_nop 1
	s_waitcnt vmcnt(15)
; __device__ __forceinline__ unsigned cvt_pk_bf16(float lo, float hi) { unsigned r; asm volatile("v_cvt_pk_bf16_f32 %0, %1, %2" : "=v"(r) : "v"(lo), "v"(hi)); return r; }
; __device__ __forceinline__ unsigned pk4_fp8(float a, float b, float c, float d) { int w = __builtin_amdgcn_cvt_pk_fp8_f32(a, b, 0, false); w = __builtin_amdgcn_cvt_pk_fp8_f32(c, d, w, true); return (unsigned)w; }
;     __device__ __forceinline__ void operator()(const f32x4 (&acc)[2][2][4][2], const pg8::Unit& u, int wr, int wc, int fr, int fq) const {
;     ...
; #pragma unroll
;             for (int m = 0; m < 4; ++m) { const int row = row0 + ai * 128 + m * 16; float ss = 0.f;
;                 u32x4 q;
; #pragma unroll
;                 for (int bj = 0; bj < 2; ++bj) { const size_t off = (size_t)row * D + col0 + bj * 8;
;                     const float asc = BASE_F32 ? 1.0f : (1.0f / 256.0f);
;                     const f32x4 v0 = acc[ai][bj][m][0] * asc + b0[m][bj], v1 = acc[ai][bj][m][1] * asc + b1[m][bj];
;                     ss += (v0[0] * v0[0] + v0[1] * v0[1]) + (v0[2] * v0[2] + v0[3] * v0[3]) + (v1[0] * v1[0] + v1[1] * v1[1]) + (v1[2] * v1[2] + v1[3] * v1[3]);
;                     u32x4 w; w.x = cvt_pk_bf16(v0[0], v0[1]); w.y = cvt_pk_bf16(v0[2], v0[3]); w.z = cvt_pk_bf16(v1[0], v1[1]); w.w = cvt_pk_bf16(v1[2], v1[3]);
;                     *(u32x4*)(out + off) = w;
;                     if (BASE_F32) { const unsigned qa = pk4_fp8(v0[0], v0[1], v0[2], v0[3]), qb = pk4_fp8(v1[0], v1[1], v1[2], v1[3]); if (bj == 0) { q.x = qa; q.y = qb; } else { q.z = qa; q.w = qb; } } }
;                 if (BASE_F32) *(u32x4*)(q8 + (size_t)row * D + col0) = q;
;                 ss += __shfl_xor(ss, 16); ss += __shfl_xor(ss, 32);
;                 if (fq == 0) ssq[(size_t)row * 16 + u.pn * 4 + wc] = ss; }
	v_pk_add_f32 v[126:127], v[52:53], v[126:127]
	v_pk_add_f32 v[124:125], v[50:51], v[124:125]
	s_waitcnt vmcnt(14)
	v_pk_add_f32 v[54:55], v[54:55], v[128:129]
	s_waitcnt vmcnt(13)
	v_pk_add_f32 v[60:61], v[60:61], v[134:135]
	v_pk_add_f32 v[58:59], v[58:59], v[132:133]
	v_pk_add_f32 v[56:57], v[56:57], v[130:131]
	s_waitcnt vmcnt(12)
	v_pk_add_f32 v[62:63], v[62:63], v[136:137]
	v_mul_f32_e32 v128, v125, v125
	v_mul_f32_e32 v129, v127, v127
	v_mul_f32_e32 v130, v55, v55
	v_cvt_pk_bf16_f32 v50, v124, v125
	v_cvt_pk_bf16_f32 v51, v126, v127
	v_cvt_pk_bf16_f32 v52, v54, v55
	v_cvt_pk_fp8_f32 v140, v124, v125
	v_cvt_pk_fp8_f32 v141, v54, v55
	v_mul_f32_e32 v55, v59, v59
	v_mul_f32_e32 v125, v61, v61
	v_pk_add_f32 v[64:65], v[64:65], v[138:139]
	v_cvt_pk_bf16_f32 v53, v56, v57
	v_mul_f32_e32 v132, v63, v63
	v_fmac_f32_e32 v128, v124, v124
	v_fmac_f32_e32 v129, v126, v126
	v_fmac_f32_e32 v55, v58, v58
	v_fmac_f32_e32 v125, v60, v60
	v_mul_f32_e32 v131, v57, v57
	v_mul_f32_e32 v133, v65, v65
	v_fmac_f32_e32 v130, v54, v54
	global_store_dwordx4 v[144:145], v[50:53], off
	v_fmac_f32_e32 v132, v62, v62
	v_add_f32_e32 v54, v55, v125
	v_add_f32_e32 v53, v128, v129
	v_fmac_f32_e32 v131, v56, v56
	v_fmac_f32_e32 v133, v64, v64
	v_add_f32_e32 v53, v53, v130
	v_add_f32_e32 v54, v54, v132
	v_add_f32_e32 v53, v131, v53
	v_add_f32_e32 v54, v133, v54
	v_add_f32_e32 v54, v53, v54
	ds_bpermute_b32 v55, v122, v54
	v_cvt_pk_fp8_f32 v142, v58, v59
	v_cvt_pk_fp8_f32 v143, v62, v63
	v_cvt_pk_bf16_f32 v50, v58, v59
	v_cvt_pk_bf16_f32 v51, v60, v61
	v_cvt_pk_bf16_f32 v52, v62, v63
	v_cvt_pk_bf16_f32 v53, v64, v65
	global_store_dwordx4 v[144:145], v[50:53], off offset:16
	v_cvt_pk_fp8_f32 v140, v126, v127 op_sel:[0,0,1]
	v_cvt_pk_fp8_f32 v141, v56, v57 op_sel:[0,0,1]
	s_waitcnt lgkmcnt(0)
	v_add_f32_e32 v50, v54, v55
	ds_bpermute_b32 v51, v123, v50
	v_cvt_pk_fp8_f32 v142, v60, v61 op_sel:[0,0,1]
	v_cvt_pk_fp8_f32 v143, v64, v65 op_sel:[0,0,1]
	v_lshlrev_b64 v[52:53], 10, v[120:121]
	v_lshl_add_u64 v[52:53], s[28:29], 0, v[52:53]
	v_lshl_add_u64 v[52:53], v[52:53], 0, v[180:181]
	global_store_dwordx4 v[52:53], v[140:143], off
	s_and_saveexec_b64 s[2:3], vcc
	s_cbranch_execz .LBB0_564
	v_lshlrev_b64 v[52:53], 6, v[120:121]
	v_lshl_add_u64 v[52:53], s[26:27], 0, v[52:53]
	v_lshl_add_u64 v[52:53], s[34:35], 2, v[52:53]
	s_lshl_b32 s20, s7, 2
	v_lshl_add_u64 v[52:53], v[52:53], 0, s[20:21]
	s_waitcnt lgkmcnt(0)
	v_add_f32_e32 v50, v50, v51
	global_store_dword v[52:53], v50, off
.LBB0_564:
	s_or_b64 exec, exec, s[2:3]
	s_waitcnt vmcnt(11)
	s_nop 4
	v_permlane32_swap_b32_e32 v110, v102
	v_permlane32_swap_b32_e32 v111, v103
	v_permlane32_swap_b32_e32 v112, v104
	v_permlane32_swap_b32_e32 v113, v105
	v_permlane32_swap_b32_e32 v106, v98
	v_permlane32_swap_b32_e32 v107, v99
	v_permlane32_swap_b32_e32 v108, v100
	v_permlane32_swap_b32_e32 v109, v101
	s_nop 1
	v_permlane16_swap_b32_e32 v110, v106
	v_permlane16_swap_b32_e32 v111, v107
	v_permlane16_swap_b32_e32 v112, v108
	v_permlane16_swap_b32_e32 v113, v109
	v_permlane16_swap_b32_e32 v102, v98
	v_permlane16_swap_b32_e32 v103, v99
	v_permlane16_swap_b32_e32 v104, v100
	v_permlane16_swap_b32_e32 v105, v101
	s_nop 1
	v_pk_add_f32 v[48:49], v[48:49], v[112:113]
	v_pk_add_f32 v[52:53], v[46:47], v[110:111]
	v_pk_add_f32 v[56:57], v[42:43], v[106:107]
	v_mul_f32_e32 v42, v53, v53
	v_mul_f32_e32 v43, v49, v49
	v_fmac_f32_e32 v42, v52, v52
	v_fmac_f32_e32 v43, v48, v48
	v_add_f32_e32 v42, v42, v43
	v_mul_f32_e32 v43, v57, v57
	v_pk_add_f32 v[54:55], v[44:45], v[108:109]
	v_fmac_f32_e32 v43, v56, v56
	s_waitcnt lgkmcnt(0)
	v_lshlrev_b64 v[50:51], 11, v[118:119]
	v_add_f32_e32 v42, v42, v43
	v_mul_f32_e32 v43, v55, v55
	v_fmac_f32_e32 v43, v54, v54
	v_lshl_add_u64 v[50:51], s[24:25], 0, v[50:51]
	v_add_f32_e32 v58, v43, v42
	v_cvt_pk_bf16_f32 v42, v52, v53
	v_cvt_pk_bf16_f32 v43, v48, v49
	v_cvt_pk_bf16_f32 v44, v56, v57
	v_cvt_pk_bf16_f32 v45, v54, v55
	v_lshl_add_u64 v[50:51], v[180:181], 1, v[50:51]
	v_pk_add_f32 v[40:41], v[40:41], v[104:105]
	v_pk_add_f32 v[38:39], v[38:39], v[102:103]
	global_store_dwordx4 v[50:51], v[42:45], off
	v_cvt_pk_fp8_f32 v46, v52, v53
	v_pk_add_f32 v[44:45], v[34:35], v[98:99]
	v_mul_f32_e32 v34, v39, v39
	v_mul_f32_e32 v35, v41, v41
	v_fmac_f32_e32 v34, v38, v38
	v_fmac_f32_e32 v35, v40, v40
	v_add_f32_e32 v34, v34, v35
	v_mul_f32_e32 v35, v45, v45
	v_pk_add_f32 v[42:43], v[36:37], v[100:101]
	v_fmac_f32_e32 v35, v44, v44
	v_add_f32_e32 v34, v34, v35
	v_mul_f32_e32 v35, v43, v43
	v_fmac_f32_e32 v35, v42, v42
	v_add_f32_e32 v34, v35, v34
	v_cvt_pk_fp8_f32 v46, v48, v49 op_sel:[0,0,1]
	v_add_f32_e32 v52, v58, v34
	v_cvt_pk_bf16_f32 v34, v38, v39
	v_cvt_pk_fp8_f32 v48, v38, v39
	ds_bpermute_b32 v38, v122, v52
	v_cvt_pk_fp8_f32 v47, v56, v57
	v_cvt_pk_fp8_f32 v49, v44, v45
	v_cvt_pk_bf16_f32 v35, v40, v41
	v_cvt_pk_bf16_f32 v36, v44, v45
	v_cvt_pk_bf16_f32 v37, v42, v43
	global_store_dwordx4 v[50:51], v[34:37], off offset:16
	v_cvt_pk_fp8_f32 v47, v54, v55 op_sel:[0,0,1]
	v_cvt_pk_fp8_f32 v48, v40, v41 op_sel:[0,0,1]
	s_waitcnt lgkmcnt(0)
	v_add_f32_e32 v34, v52, v38
	ds_bpermute_b32 v35, v123, v34
	v_cvt_pk_fp8_f32 v49, v42, v43 op_sel:[0,0,1]
	v_lshlrev_b64 v[36:37], 10, v[118:119]
	v_lshl_add_u64 v[36:37], s[28:29], 0, v[36:37]
	v_lshl_add_u64 v[36:37], v[36:37], 0, v[180:181]
	global_store_dwordx4 v[36:37], v[46:49], off
	s_and_saveexec_b64 s[2:3], vcc
	s_cbranch_execz .LBB0_566
	v_lshlrev_b64 v[36:37], 6, v[118:119]
	v_lshl_add_u64 v[36:37], s[26:27], 0, v[36:37]
	v_lshl_add_u64 v[36:37], s[34:35], 2, v[36:37]
	s_lshl_b32 s20, s7, 2
	v_lshl_add_u64 v[36:37], v[36:37], 0, s[20:21]
	s_waitcnt lgkmcnt(0)
	v_add_f32_e32 v34, v34, v35
	global_store_dword v[36:37], v34, off
; __device__ __forceinline__ unsigned cvt_pk_bf16(float lo, float hi) { unsigned r; asm volatile("v_cvt_pk_bf16_f32 %0, %1, %2" : "=v"(r) : "v"(lo), "v"(hi)); return r; }
; __device__ __forceinline__ unsigned pk4_fp8(float a, float b, float c, float d) { int w = __builtin_amdgcn_cvt_pk_fp8_f32(a, b, 0, false); w = __builtin_amdgcn_cvt_pk_fp8_f32(c, d, w, true); return (unsigned)w; }
;     __device__ __forceinline__ void operator()(const f32x4 (&acc)[2][2][4][2], const pg8::Unit& u, int wr, int wc, int fr, int fq) const {
;     ...
; #pragma unroll
;             for (int m = 0; m < 4; ++m) { const int row = row0 + ai * 128 + m * 16; float ss = 0.f;
;                 u32x4 q;
; #pragma unroll
;                 for (int bj = 0; bj < 2; ++bj) { const size_t off = (size_t)row * D + col0 + bj * 8;
;                     const float asc = BASE_F32 ? 1.0f : (1.0f / 256.0f);
;                     const f32x4 v0 = acc[ai][bj][m][0] * asc + b0[m][bj], v1 = acc[ai][bj][m][1] * asc + b1[m][bj];
;                     ss += (v0[0] * v0[0] + v0[1] * v0[1]) + (v0[2] * v0[2] + v0[3] * v0[3]) + (v1[0] * v1[0] + v1[1] * v1[1]) + (v1[2] * v1[2] + v1[3] * v1[3]);
;                     u32x4 w; w.x = cvt_pk_bf16(v0[0], v0[1]); w.y = cvt_pk_bf16(v0[2], v0[3]); w.z = cvt_pk_bf16(v1[0], v1[1]); w.w = cvt_pk_bf16(v1[2], v1[3]);
;                     *(u32x4*)(out + off) = w;
;                     if (BASE_F32) { const unsigned qa = pk4_fp8(v0[0], v0[1], v0[2], v0[3]), qb = pk4_fp8(v1[0], v1[1], v1[2], v1[3]); if (bj == 0) { q.x = qa; q.y = qb; } else { q.z = qa; q.w = qb; } } }
;                 if (BASE_F32) *(u32x4*)(q8 + (size_t)row * D + col0) = q;
;                 ss += __shfl_xor(ss, 16); ss += __shfl_xor(ss, 32);
;                 if (fq == 0) ssq[(size_t)row * 16 + u.pn * 4 + wc] = ss; }
.LBB0_566:
	s_or_b64 exec, exec, s[2:3]
	s_waitcnt vmcnt(10)
	s_nop 4
	v_permlane32_swap_b32_e32 v94, v86
	v_permlane32_swap_b32_e32 v95, v87
	v_permlane32_swap_b32_e32 v96, v88
	v_permlane32_swap_b32_e32 v97, v89
	v_permlane32_swap_b32_e32 v90, v82
	v_permlane32_swap_b32_e32 v91, v83
	v_permlane32_swap_b32_e32 v92, v84
	v_permlane32_swap_b32_e32 v93, v85
	s_nop 1
	v_permlane16_swap_b32_e32 v94, v90
	v_permlane16_swap_b32_e32 v95, v91
	v_permlane16_swap_b32_e32 v96, v92
	v_permlane16_swap_b32_e32 v97, v93
	v_permlane16_swap_b32_e32 v86, v82
	v_permlane16_swap_b32_e32 v87, v83
	v_permlane16_swap_b32_e32 v88, v84
	v_permlane16_swap_b32_e32 v89, v85
	s_nop 1
	v_pk_add_f32 v[32:33], v[32:33], v[96:97]
	v_pk_add_f32 v[36:37], v[30:31], v[94:95]
	v_pk_add_f32 v[40:41], v[26:27], v[90:91]
	v_mul_f32_e32 v26, v37, v37
	v_mul_f32_e32 v27, v33, v33
	v_fmac_f32_e32 v26, v36, v36
	v_fmac_f32_e32 v27, v32, v32
	v_add_f32_e32 v26, v26, v27
	v_mul_f32_e32 v27, v41, v41
	v_pk_add_f32 v[38:39], v[28:29], v[92:93]
	v_fmac_f32_e32 v27, v40, v40
	s_waitcnt lgkmcnt(0)
	v_lshlrev_b64 v[34:35], 11, v[116:117]
	v_add_f32_e32 v26, v26, v27
	v_mul_f32_e32 v27, v39, v39
	v_fmac_f32_e32 v27, v38, v38
	v_lshl_add_u64 v[34:35], s[24:25], 0, v[34:35]
	v_add_f32_e32 v42, v27, v26
	v_cvt_pk_bf16_f32 v26, v36, v37
	v_cvt_pk_bf16_f32 v27, v32, v33
	v_cvt_pk_bf16_f32 v28, v40, v41
	v_cvt_pk_bf16_f32 v29, v38, v39
	v_lshl_add_u64 v[34:35], v[180:181], 1, v[34:35]
	v_pk_add_f32 v[24:25], v[24:25], v[88:89]
	v_pk_add_f32 v[22:23], v[22:23], v[86:87]
	global_store_dwordx4 v[34:35], v[26:29], off
	v_cvt_pk_fp8_f32 v30, v36, v37
	v_pk_add_f32 v[28:29], v[18:19], v[82:83]
	v_mul_f32_e32 v18, v23, v23
	v_mul_f32_e32 v19, v25, v25
	v_fmac_f32_e32 v18, v22, v22
	v_fmac_f32_e32 v19, v24, v24
	v_add_f32_e32 v18, v18, v19
	v_mul_f32_e32 v19, v29, v29
	v_pk_add_f32 v[26:27], v[20:21], v[84:85]
	v_fmac_f32_e32 v19, v28, v28
	v_add_f32_e32 v18, v18, v19
	v_mul_f32_e32 v19, v27, v27
	v_fmac_f32_e32 v19, v26, v26
	v_add_f32_e32 v18, v19, v18
	v_cvt_pk_fp8_f32 v30, v32, v33 op_sel:[0,0,1]
	v_add_f32_e32 v36, v42, v18
	v_cvt_pk_bf16_f32 v18, v22, v23
	v_cvt_pk_fp8_f32 v32, v22, v23
	ds_bpermute_b32 v22, v122, v36
	v_cvt_pk_fp8_f32 v31, v40, v41
	v_cvt_pk_fp8_f32 v33, v28, v29
	v_cvt_pk_bf16_f32 v19, v24, v25
	v_cvt_pk_bf16_f32 v20, v28, v29
	v_cvt_pk_bf16_f32 v21, v26, v27
	global_store_dwordx4 v[34:35], v[18:21], off offset:16
	v_cvt_pk_fp8_f32 v31, v38, v39 op_sel:[0,0,1]
	v_cvt_pk_fp8_f32 v32, v24, v25 op_sel:[0,0,1]
	s_waitcnt lgkmcnt(0)
	v_add_f32_e32 v18, v36, v22
	ds_bpermute_b32 v19, v123, v18
	v_cvt_pk_fp8_f32 v33, v26, v27 op_sel:[0,0,1]
	v_lshlrev_b64 v[20:21], 10, v[116:117]
	v_lshl_add_u64 v[20:21], s[28:29], 0, v[20:21]
	v_lshl_add_u64 v[20:21], v[20:21], 0, v[180:181]
	global_store_dwordx4 v[20:21], v[30:33], off
	s_and_saveexec_b64 s[2:3], vcc
	s_cbranch_execz .LBB0_568
	v_lshlrev_b64 v[20:21], 6, v[116:117]
	v_lshl_add_u64 v[20:21], s[26:27], 0, v[20:21]
	v_lshl_add_u64 v[20:21], s[34:35], 2, v[20:21]
	s_lshl_b32 s20, s7, 2
	v_lshl_add_u64 v[20:21], v[20:21], 0, s[20:21]
	s_waitcnt lgkmcnt(0)
	v_add_f32_e32 v18, v18, v19
	global_store_dword v[20:21], v18, off
.LBB0_568:
	s_or_b64 exec, exec, s[2:3]
	s_waitcnt vmcnt(9)
	s_nop 4
	v_permlane32_swap_b32_e32 v78, v70
	v_permlane32_swap_b32_e32 v79, v71
	v_permlane32_swap_b32_e32 v80, v72
	v_permlane32_swap_b32_e32 v81, v73
	v_permlane32_swap_b32_e32 v74, v66
	v_permlane32_swap_b32_e32 v75, v67
	v_permlane32_swap_b32_e32 v76, v68
	v_permlane32_swap_b32_e32 v77, v69
	s_nop 1
	v_permlane16_swap_b32_e32 v78, v74
	v_permlane16_swap_b32_e32 v79, v75
	v_permlane16_swap_b32_e32 v80, v76
	v_permlane16_swap_b32_e32 v81, v77
	v_permlane16_swap_b32_e32 v70, v66
	v_permlane16_swap_b32_e32 v71, v67
	v_permlane16_swap_b32_e32 v72, v68
	v_permlane16_swap_b32_e32 v73, v69
	s_nop 1
	v_pk_add_f32 v[16:17], v[16:17], v[80:81]
	v_pk_add_f32 v[20:21], v[14:15], v[78:79]
	v_pk_add_f32 v[24:25], v[10:11], v[74:75]
	v_mul_f32_e32 v10, v21, v21
	v_mul_f32_e32 v11, v17, v17
	v_fmac_f32_e32 v10, v20, v20
	v_fmac_f32_e32 v11, v16, v16
	v_add_f32_e32 v10, v10, v11
	v_mul_f32_e32 v11, v25, v25
	v_pk_add_f32 v[22:23], v[12:13], v[76:77]
	v_fmac_f32_e32 v11, v24, v24
	s_waitcnt lgkmcnt(0)
	v_lshlrev_b64 v[18:19], 11, v[114:115]
	v_add_f32_e32 v10, v10, v11
	v_mul_f32_e32 v11, v23, v23
	v_fmac_f32_e32 v11, v22, v22
	v_lshl_add_u64 v[18:19], s[24:25], 0, v[18:19]
	v_add_f32_e32 v26, v11, v10
	v_cvt_pk_bf16_f32 v10, v20, v21
	v_cvt_pk_bf16_f32 v11, v16, v17
	v_cvt_pk_bf16_f32 v12, v24, v25
	v_cvt_pk_bf16_f32 v13, v22, v23
	v_lshl_add_u64 v[18:19], v[180:181], 1, v[18:19]
	v_pk_add_f32 v[8:9], v[8:9], v[72:73]
	v_pk_add_f32 v[6:7], v[6:7], v[70:71]
	global_store_dwordx4 v[18:19], v[10:13], off
	v_cvt_pk_fp8_f32 v14, v20, v21
	v_pk_add_f32 v[12:13], v[2:3], v[66:67]
	v_mul_f32_e32 v2, v7, v7
	v_mul_f32_e32 v3, v9, v9
	v_fmac_f32_e32 v2, v6, v6
	v_fmac_f32_e32 v3, v8, v8
	v_add_f32_e32 v2, v2, v3
	v_mul_f32_e32 v3, v13, v13
	v_pk_add_f32 v[10:11], v[4:5], v[68:69]
	v_fmac_f32_e32 v3, v12, v12
	v_add_f32_e32 v2, v2, v3
	v_mul_f32_e32 v3, v11, v11
	v_fmac_f32_e32 v3, v10, v10
	v_add_f32_e32 v2, v3, v2
	v_cvt_pk_fp8_f32 v14, v16, v17 op_sel:[0,0,1]
	v_add_f32_e32 v20, v26, v2
	v_cvt_pk_bf16_f32 v2, v6, v7
	v_cvt_pk_fp8_f32 v16, v6, v7
	ds_bpermute_b32 v6, v122, v20
	v_cvt_pk_fp8_f32 v15, v24, v25
	v_cvt_pk_fp8_f32 v17, v12, v13
	v_cvt_pk_bf16_f32 v3, v8, v9
	v_cvt_pk_bf16_f32 v4, v12, v13
	v_cvt_pk_bf16_f32 v5, v10, v11
	global_store_dwordx4 v[18:19], v[2:5], off offset:16
	v_cvt_pk_fp8_f32 v15, v22, v23 op_sel:[0,0,1]
	v_cvt_pk_fp8_f32 v16, v8, v9 op_sel:[0,0,1]
	s_waitcnt lgkmcnt(0)
	v_add_f32_e32 v2, v20, v6
	ds_bpermute_b32 v3, v123, v2
	v_cvt_pk_fp8_f32 v17, v10, v11 op_sel:[0,0,1]
	v_lshlrev_b64 v[4:5], 10, v[114:115]
	v_lshl_add_u64 v[4:5], s[28:29], 0, v[4:5]
	v_lshl_add_u64 v[4:5], v[4:5], 0, v[180:181]
	global_store_dwordx4 v[4:5], v[14:17], off
	s_and_saveexec_b64 s[2:3], vcc
	s_cbranch_execz .LBB0_570
	v_lshlrev_b64 v[4:5], 6, v[114:115]
	v_lshl_add_u64 v[4:5], s[26:27], 0, v[4:5]
	v_lshl_add_u64 v[4:5], s[34:35], 2, v[4:5]
	s_lshl_b32 s20, s7, 2
	v_lshl_add_u64 v[4:5], v[4:5], 0, s[20:21]
	s_waitcnt lgkmcnt(0)
	v_add_f32_e32 v2, v2, v3
	global_store_dword v[4:5], v2, off
